# bundle9 + attention: one static s_setprio 1 for waves 4-7 before the loop (younger-half priority raise)
# speedup vs baseline: 1.0070x; 1.0070x over previous
.LBB0_411:
	s_or_b64 exec, exec, s[56:57]
	v_readlane_b32 s23, v254, 12
	s_mov_b32 s70, s59
	s_waitcnt lgkmcnt(0)
	s_barrier
	v_mbcnt_lo_u32_b32 v49, -1, 0
	v_mbcnt_hi_u32_b32 v49, -1, v49
	s_lshr_b32 s6, s70, 5
	s_and_b32 s7, s70, 31
	s_mulk_i32 s6, 0xc00
	s_or_b32 s24, s6, s7
	s_mul_hi_i32 s6, s24, 0x2aaaaaab
	s_lshr_b32 s8, s6, 31
	s_ashr_i32 s6, s6, 5
	s_add_i32 s8, s6, s8
	s_mul_i32 s6, s8, 0xffffff40
	s_add_i32 s6, s6, s24
	s_ashr_i32 s30, s6, 6
	s_ashr_i32 s10, s8, 4
	s_cmp_eq_u32 s30, 1
	s_cselect_b32 s9, 3, 15
	s_cselect_b32 s11, 2, 4
	s_cmp_lt_u32 s6, 64
	s_cselect_b32 s12, 0, s11
	s_cselect_b32 s6, 0, s9
	s_lshr_b32 s25, s7, s12
	v_lshl_add_u32 v50, s23, 6, v49
	v_sub_u32_e64 v0, s25, 1 clamp
	s_ashr_i32 s9, s8, 31
	v_lshlrev_b32_e32 v4, 7, v0
	v_bfe_u32 v172, v50, 3, 7
	s_and_b32 s13, s6, s70
	s_lshl_b64 s[6:7], s[8:9], 13
	v_or_b32_e32 v0, v4, v172
	s_or_b32 s6, s6, s13
	v_lshlrev_b32_e32 v51, 3, v49
	v_lshlrev_b32_e32 v64, s12, v0
	v_and_b32_e32 v48, 56, v51
	v_lshl_add_u64 v[0:1], s[6:7], 0, v[64:65]
	v_lshlrev_b64 v[0:1], 7, v[0:1]
	v_lshlrev_b32_e32 v5, 1, v48
	v_or_b32_e32 v0, v0, v5
	v_add_u32_e32 v52, 0x200, v50
	v_lshl_add_u64 v[2:3], s[76:77], 0, v[0:1]
	v_lshl_add_u64 v[0:1], s[78:79], 0, v[0:1]
	v_bfe_u32 v174, v52, 3, 7
	s_barrier
	global_load_dwordx4 v[16:19], v[2:3], off
	global_load_dwordx4 v[20:23], v[0:1], off
	v_or_b32_e32 v0, v4, v174
	v_lshlrev_b32_e32 v64, s12, v0
	v_lshl_add_u64 v[0:1], s[6:7], 0, v[64:65]
	v_lshlrev_b64 v[0:1], 7, v[0:1]
	v_or_b32_e32 v0, v0, v5
	v_lshl_add_u64 v[2:3], s[76:77], 0, v[0:1]
	v_lshl_add_u64 v[0:1], s[78:79], 0, v[0:1]
	s_lshl_b32 s14, s25, 7
	global_load_dwordx4 v[24:27], v[2:3], off
	global_load_dwordx4 v[28:31], v[0:1], off
	v_or_b32_e32 v0, s14, v172
	v_lshlrev_b32_e32 v64, s12, v0
	v_lshl_add_u64 v[0:1], s[6:7], 0, v[64:65]
	v_lshlrev_b64 v[0:1], 7, v[0:1]
	v_or_b32_e32 v0, v0, v5
	v_add_u32_e32 v53, 0x600, v50
	v_lshl_add_u64 v[2:3], s[76:77], 0, v[0:1]
	v_lshl_add_u64 v[0:1], s[78:79], 0, v[0:1]
	v_bfe_u32 v175, v53, 3, 7
	global_load_dwordx4 v[32:35], v[2:3], off
	global_load_dwordx4 v[36:39], v[0:1], off
	v_or_b32_e32 v0, s14, v175
	v_lshlrev_b32_e32 v64, s12, v0
	v_lshl_add_u64 v[0:1], s[6:7], 0, v[64:65]
	v_lshlrev_b64 v[0:1], 7, v[0:1]
	v_or_b32_e32 v0, v0, v5
	v_bfe_u32 v56, v49, 4, 2
	v_lshl_add_u64 v[2:3], s[76:77], 0, v[0:1]
	v_lshl_add_u64 v[0:1], s[78:79], 0, v[0:1]
	v_and_b32_e32 v55, 15, v49
	v_lshlrev_b32_e32 v57, 2, v56
	global_load_dwordx4 v[40:43], v[2:3], off
	global_load_dwordx4 v[44:47], v[0:1], off
	v_cmp_lt_u32_e32 vcc, v57, v55
	v_mov_b32_e32 v8, 0xfe967699
	v_cmp_gt_u32_e64 s[6:7], v57, v55
	v_or_b32_e32 v1, 1, v57
	v_or_b32_e32 v2, 2, v57
	v_cndmask_b32_e32 v4, 0, v8, vcc
	v_cndmask_b32_e64 v0, 0, v8, s[6:7]
	v_cmp_lt_u32_e64 s[6:7], v1, v55
	v_cndmask_b32_e64 v1, v8, 0, vcc
	v_cmp_lt_u32_e32 vcc, v2, v55
	v_or_b32_e32 v3, 3, v57
	s_ashr_i32 s11, s10, 31
	v_cndmask_b32_e32 v6, 0, v8, vcc
	v_cmp_gt_u32_e32 vcc, v2, v55
	v_cndmask_b32_e64 v5, 0, v8, s[6:7]
	s_lshl_b64 s[6:7], s[10:11], 13
	v_cndmask_b32_e32 v2, 0, v8, vcc
	v_cmp_lt_u32_e32 vcc, v3, v55
	s_lshl_b32 s10, s23, 4
	s_add_i32 s14, s14, s10
	v_cndmask_b32_e32 v7, 0, v8, vcc
	v_cmp_gt_u32_e32 vcc, v3, v55
	s_or_b32 s6, s6, s13
	v_and_b32_e32 v160, 48, v49
	v_lshrrev_b32_e32 v204, 2, v55
	v_lshrrev_b32_e32 v205, 3, v55
	v_xor_b32_e32 v204, v204, v205
	v_and_b32_e32 v204, 1, v204
	v_lshlrev_b32_e32 v204, 4, v204
	v_xor_b32_e32 v215, v160, v204
	v_cndmask_b32_e32 v3, 0, v8, vcc
	v_or_b32_e32 v8, s14, v55
	v_ashrrev_i32_e32 v9, 31, v8
	v_lshlrev_b64 v[8:9], s12, v[8:9]
	v_lshl_add_u64 v[166:167], s[6:7], 0, v[8:9]
	s_lshl_b64 s[6:7], s[8:9], 20
	s_add_u32 s6, s64, s6
	v_lshlrev_b32_e32 v8, 7, v166
	s_addc_u32 s7, s65, s7
	v_and_b32_e32 v64, 0xfff80, v8
	v_lshl_add_u64 v[8:9], s[6:7], 0, v[64:65]
	v_mov_b32_e32 v161, v65
	v_lshl_add_u64 v[12:13], v[8:9], 0, v[160:161]
	global_load_dwordx4 v[8:11], v[12:13], off
	s_nop 0
	global_load_dwordx4 v[12:15], v[12:13], off offset:64
	v_lshrrev_b32_e32 v58, 3, v50
	v_add_u32_e32 v59, 0x400, v50
	v_lshlrev_b32_e32 v50, 3, v56
	v_lshlrev_b32_e32 v56, 4, v49
	s_movk_i32 s26, 0x90
	v_lshrrev_b32_e32 v52, 3, v52
	v_and_b32_e32 v176, 0x70, v56
	v_lshrrev_b32_e32 v204, 2, v58
	v_lshrrev_b32_e32 v205, 3, v58
	v_xor_b32_e32 v204, v204, v205
	v_and_b32_e32 v204, 1, v204
	v_lshlrev_b32_e32 v204, 4, v204
	v_xor_b32_e32 v176, v176, v204
	v_mul_lo_u32 v177, v58, s26
	v_add3_u32 v56, 0, v177, v176
	v_mul_lo_u32 v178, v52, s26
	s_waitcnt vmcnt(0)
	ds_write_b128 v56, v[16:19]
	ds_write_b128 v56, v[20:23] offset:36864
	v_add3_u32 v16, 0, v178, v176
	s_add_i32 s6, s10, 16
	ds_write_b128 v16, v[24:27]
	ds_write_b128 v16, v[28:31] offset:36864
	v_lshrrev_b32_e32 v16, 3, v59
	v_or_b32_e32 v17, s6, v55
	s_add_i32 s6, s10, 32
	v_lshrrev_b32_e32 v53, 3, v53
	v_mul_lo_u32 v179, v16, s26
	v_mul_lo_u32 v183, v17, s26
	v_or_b32_e32 v17, s6, v55
	s_add_i32 s6, s10, 48
	v_add3_u32 v16, 0, v179, v176
	v_mul_lo_u32 v180, v53, s26
	v_mul_lo_u32 v184, v17, s26
	v_or_b32_e32 v17, s6, v55
	s_add_i32 s6, s10, 64
	ds_write_b128 v16, v[32:35]
	ds_write_b128 v16, v[36:39] offset:36864
	v_add3_u32 v16, 0, v180, v176
	v_mul_lo_u32 v185, v17, s26
	v_or_b32_e32 v17, s6, v55
	s_add_i32 s6, s10, 0x50
	ds_write_b128 v16, v[40:43]
	ds_write_b128 v16, v[44:47] offset:36864
	v_bfe_u32 v16, v49, 2, 2
	v_mul_lo_u32 v186, v17, s26
	v_or_b32_e32 v17, s6, v55
	s_add_i32 s6, s10, 0x60
	s_and_b32 s22, s8, 15
	v_or_b32_e32 v181, s10, v55
	v_or3_b32 v16, v16, s10, v57
	v_mul_lo_u32 v187, v17, s26
	v_or_b32_e32 v17, s6, v55
	s_add_i32 s6, s10, 0x70
	s_addk_i32 s10, 0x80
	s_cmp_lt_i32 s23, 8
	s_cselect_b64 s[20:21], -1, 0
	s_cmp_lt_i32 s23, 7
	s_cselect_b64 s[18:19], -1, 0
	s_cmp_lt_i32 s23, 6
	s_cselect_b64 s[16:17], -1, 0
	s_cmp_lt_i32 s23, 5
	s_cselect_b64 s[14:15], -1, 0
	s_cmp_lt_i32 s23, 4
	v_mul_lo_u32 v188, v17, s26
	v_or_b32_e32 v17, s6, v55
	s_cselect_b64 s[12:13], -1, 0
	s_cmp_lt_i32 s23, 3
	v_mul_lo_u32 v189, v17, s26
	v_or_b32_e32 v17, s10, v55
	s_cselect_b64 s[10:11], -1, 0
	s_cmp_lt_i32 s23, 2
	v_and_b32_e32 v54, 63, v49
	s_cselect_b64 s[8:9], -1, 0
	s_cmp_lt_i32 s23, 1
	s_mov_b32 s71, s63
	s_mov_b32 s38, 0
	v_and_b32_e32 v171, 24, v51
	v_lshrrev_b32_e32 v204, 4, v49
	v_lshrrev_b32_e32 v205, 5, v49
	v_xor_b32_e32 v204, v204, v205
	v_and_b32_e32 v204, 1, v204
	v_lshlrev_b32_e32 v204, 4, v204
	v_xor_b32_e32 v171, v171, v204
	v_cmp_gt_u32_e32 vcc, 16, v54
	v_mul_lo_u32 v182, v181, s26
	v_mul_lo_u32 v190, v17, s26
	s_cselect_b64 s[6:7], -1, 0
	v_mul_lo_u32 v173, v16, s26
	s_or_b32 s39, s24, 32
	v_lshlrev_b32_e32 v191, 1, v48
	v_lshlrev_b32_e32 v168, 1, v50
	s_waitcnt lgkmcnt(0)
	s_barrier
	v_readlane_b32 s100, v254, 12
	s_nop 3
	s_cmp_lt_i32 s100, 4
	s_cbranch_scc1 .Laprio_done
	s_setprio 1
.Laprio_done:
.LBB0_412:
	s_mul_hi_i32 s23, s39, 0x2aaaaaab
	s_lshr_b32 s24, s23, 31
	s_ashr_i32 s23, s23, 5
	s_add_i32 s34, s23, s24
	s_mul_i32 s23, s34, 0xffffff40
	s_add_i32 s23, s39, s23
	s_mov_b32 s31, s25
	s_and_b32 s49, s38, 1
	s_ashr_i32 s24, s23, 6
	s_and_b32 s25, s39, 63
	s_ashr_i32 s36, s34, 4
	s_cmp_eq_u32 s24, 1
	s_cselect_b64 s[26:27], -1, 0
	s_and_b64 s[28:29], s[26:27], exec
	s_cselect_b32 s35, 3, 15
	s_cselect_b32 s37, 2, 4
	s_cmp_lt_u32 s23, 64
	s_cselect_b64 s[28:29], -1, 0
	s_and_b64 s[56:57], s[28:29], exec
	s_cselect_b32 s62, 0, s37
	s_waitcnt vmcnt(2)
	v_mov_b64_e32 v[88:89], v[10:11]
	s_cselect_b32 s23, 0, s35
	s_lshr_b32 s25, s25, s62
	s_waitcnt vmcnt(1)
	v_mov_b64_e32 v[50:51], v[14:15]
	v_mov_b64_e32 v[86:87], v[8:9]
	v_sub_u32_e64 v8, s25, 1 clamp
	v_mov_b64_e32 v[48:49], v[12:13]
	s_ashr_i32 s35, s34, 31
	v_lshlrev_b32_e32 v12, 7, v8
	s_and_b32 s23, s23, s70
	s_lshl_b64 s[56:57], s[34:35], 13
	v_or_b32_e32 v8, v12, v172
	s_or_b32 s56, s56, s23
	v_lshlrev_b32_e32 v64, s62, v8
	v_lshl_add_u64 v[8:9], s[56:57], 0, v[64:65]
	v_lshlrev_b64 v[8:9], 7, v[8:9]
	v_or_b32_e32 v8, v8, v191
	v_lshl_add_u64 v[10:11], s[76:77], 0, v[8:9]
	v_lshl_add_u64 v[8:9], s[78:79], 0, v[8:9]
	global_load_dwordx4 v[16:19], v[10:11], off
	global_load_dwordx4 v[20:23], v[8:9], off
	v_or_b32_e32 v8, v12, v174
	v_lshlrev_b32_e32 v64, s62, v8
	v_lshl_add_u64 v[8:9], s[56:57], 0, v[64:65]
	v_lshlrev_b64 v[8:9], 7, v[8:9]
	v_or_b32_e32 v8, v8, v191
	v_lshl_add_u64 v[10:11], s[76:77], 0, v[8:9]
	v_lshl_add_u64 v[8:9], s[78:79], 0, v[8:9]
	s_lshl_b32 s63, s25, 7
	global_load_dwordx4 v[24:27], v[10:11], off
	global_load_dwordx4 v[28:31], v[8:9], off
	v_or_b32_e32 v8, s63, v172
	v_lshlrev_b32_e32 v64, s62, v8
	v_lshl_add_u64 v[8:9], s[56:57], 0, v[64:65]
	v_lshlrev_b64 v[8:9], 7, v[8:9]
	v_or_b32_e32 v8, v8, v191
	v_lshl_add_u64 v[10:11], s[76:77], 0, v[8:9]
	v_lshl_add_u64 v[8:9], s[78:79], 0, v[8:9]
	global_load_dwordx4 v[32:35], v[10:11], off
	global_load_dwordx4 v[36:39], v[8:9], off
	v_or_b32_e32 v8, s63, v175
	v_lshlrev_b32_e32 v64, s62, v8
	v_lshl_add_u64 v[8:9], s[56:57], 0, v[64:65]
	v_lshlrev_b64 v[8:9], 7, v[8:9]
	v_or_b32_e32 v8, v8, v191
	v_lshl_add_u64 v[10:11], s[76:77], 0, v[8:9]
	v_lshl_add_u64 v[8:9], s[78:79], 0, v[8:9]
	global_load_dwordx4 v[40:43], v[10:11], off
	global_load_dwordx4 v[44:47], v[8:9], off
	s_ashr_i32 s37, s36, 31
	v_add_u32_e32 v8, s63, v181
	s_lshl_b64 s[36:37], s[36:37], 13
	v_ashrrev_i32_e32 v9, 31, v8
	s_or_b32 s36, s36, s23
	v_lshlrev_b64 v[8:9], s62, v[8:9]
	v_lshl_add_u64 v[164:165], s[36:37], 0, v[8:9]
	v_lshlrev_b64 v[162:163], 6, v[164:165]
	s_lshl_b64 s[36:37], s[34:35], 20
	s_add_u32 s36, s64, s36
	v_lshlrev_b32_e32 v8, 1, v162
	s_addc_u32 s37, s65, s37
	v_and_b32_e32 v64, 0xfff80, v8
	v_lshl_add_u64 v[8:9], s[36:37], 0, v[64:65]
	v_mov_b32_e32 v169, v65
	v_lshl_add_u64 v[12:13], v[8:9], 0, v[168:169]
	global_load_dwordx4 v[8:11], v[12:13], off
	s_nop 0
	global_load_dwordx4 v[12:15], v[12:13], off offset:64
	s_mul_i32 s23, s49, 0x12000
	s_add_i32 s23, s23, 0
	v_add3_u32 v56, s23, v182, v215
	v_add3_u32 v64, s23, v183, v215
	ds_read_b128 v[52:55], v56
	ds_read_b128 v[56:59], v56 offset:64
	ds_read_b128 v[60:63], v64
	ds_read_b128 v[66:69], v64 offset:64
	v_add3_u32 v64, s23, v184, v215
	ds_read_b128 v[70:73], v64
	ds_read_b128 v[74:77], v64 offset:64
	v_add3_u32 v64, s23, v185, v215
	ds_read_b128 v[90:93], v64
	ds_read_b128 v[94:97], v64 offset:64
	v_add3_u32 v64, s23, v186, v215
	ds_read_b128 v[98:101], v64
	ds_read_b128 v[102:105], v64 offset:64
	v_add3_u32 v64, s23, v187, v215
	ds_read_b128 v[106:109], v64
	ds_read_b128 v[110:113], v64 offset:64
	v_add3_u32 v64, s23, v188, v215
	ds_read_b128 v[114:117], v64
	ds_read_b128 v[118:121], v64 offset:64
	v_add3_u32 v64, s23, v189, v215
	ds_read_b128 v[122:125], v64
	ds_read_b128 v[126:129], v64 offset:64
	v_add3_u32 v64, s23, v190, v215
	ds_read_b128 v[130:133], v64
	ds_read_b128 v[134:137], v64 offset:64
	s_waitcnt lgkmcnt(14)
	v_mfma_f32_16x16x32_bf16 v[52:55], v[52:55], v[86:89], v[4:7]
	s_cmp_lg_u32 s31, 0
	v_mfma_f32_16x16x32_bf16 v[82:85], v[56:59], v[48:51], v[52:55]
	v_mfma_f32_16x16x32_bf16 v[52:55], v[60:63], v[86:89], 0
	v_mfma_f32_16x16x32_bf16 v[78:81], v[66:69], v[48:51], v[52:55]
	s_waitcnt lgkmcnt(13)
	v_mfma_f32_16x16x32_bf16 v[52:55], v[70:73], v[86:89], 0
	s_waitcnt lgkmcnt(12)
	v_mfma_f32_16x16x32_bf16 v[74:77], v[74:77], v[48:51], v[52:55]
	s_waitcnt lgkmcnt(11)
	v_mfma_f32_16x16x32_bf16 v[52:55], v[90:93], v[86:89], 0
	s_waitcnt lgkmcnt(10)
	v_mfma_f32_16x16x32_bf16 v[70:73], v[94:97], v[48:51], v[52:55]
	s_waitcnt lgkmcnt(9)
	v_mfma_f32_16x16x32_bf16 v[52:55], v[98:101], v[86:89], 0
	s_waitcnt lgkmcnt(8)
	v_mfma_f32_16x16x32_bf16 v[66:69], v[102:105], v[48:51], v[52:55]
	s_waitcnt lgkmcnt(7)
	v_mfma_f32_16x16x32_bf16 v[52:55], v[106:109], v[86:89], 0
	s_waitcnt lgkmcnt(6)
	v_mfma_f32_16x16x32_bf16 v[60:63], v[110:113], v[48:51], v[52:55]
	s_waitcnt lgkmcnt(5)
	v_mfma_f32_16x16x32_bf16 v[52:55], v[114:117], v[86:89], 0
	s_waitcnt lgkmcnt(4)
	v_mfma_f32_16x16x32_bf16 v[56:59], v[118:121], v[48:51], v[52:55]
	s_waitcnt lgkmcnt(3)
	v_mfma_f32_16x16x32_bf16 v[52:55], v[122:125], v[86:89], 0
	s_waitcnt lgkmcnt(1)
	v_mfma_f32_16x16x32_bf16 v[86:89], v[130:133], v[86:89], v[0:3]
	v_mfma_f32_16x16x32_bf16 v[52:55], v[126:129], v[48:51], v[52:55]
	s_waitcnt lgkmcnt(0)
	v_mfma_f32_16x16x32_bf16 v[48:51], v[134:137], v[48:51], v[86:89]
	s_cbranch_scc1 .LBB0_414
	s_nop 3
	v_pk_add_f32 v[86:87], v[84:85], s[84:85] op_sel_hi:[1,0]
	v_pk_add_f32 v[88:89], v[82:83], s[84:85] op_sel_hi:[1,0]
	v_cndmask_b32_e64 v85, v85, v87, s[20:21]
	v_cndmask_b32_e64 v84, v84, v86, s[20:21]
	v_cndmask_b32_e64 v83, v83, v89, s[20:21]
	v_cndmask_b32_e64 v82, v82, v88, s[20:21]
	v_pk_add_f32 v[86:87], v[80:81], s[84:85] op_sel_hi:[1,0]
	v_pk_add_f32 v[88:89], v[78:79], s[84:85] op_sel_hi:[1,0]
	v_cndmask_b32_e64 v81, v81, v87, s[18:19]
	v_cndmask_b32_e64 v80, v80, v86, s[18:19]
	v_cndmask_b32_e64 v79, v79, v89, s[18:19]
	v_cndmask_b32_e64 v78, v78, v88, s[18:19]
	v_pk_add_f32 v[86:87], v[76:77], s[84:85] op_sel_hi:[1,0]
	v_pk_add_f32 v[88:89], v[74:75], s[84:85] op_sel_hi:[1,0]
	v_cndmask_b32_e64 v77, v77, v87, s[16:17]
	v_cndmask_b32_e64 v76, v76, v86, s[16:17]
	v_cndmask_b32_e64 v75, v75, v89, s[16:17]
	v_cndmask_b32_e64 v74, v74, v88, s[16:17]
	v_pk_add_f32 v[86:87], v[72:73], s[84:85] op_sel_hi:[1,0]
	v_pk_add_f32 v[88:89], v[70:71], s[84:85] op_sel_hi:[1,0]
	v_cndmask_b32_e64 v73, v73, v87, s[14:15]
	v_cndmask_b32_e64 v72, v72, v86, s[14:15]
	v_cndmask_b32_e64 v71, v71, v89, s[14:15]
	v_cndmask_b32_e64 v70, v70, v88, s[14:15]
	v_pk_add_f32 v[86:87], v[68:69], s[84:85] op_sel_hi:[1,0]
	v_pk_add_f32 v[88:89], v[66:67], s[84:85] op_sel_hi:[1,0]
	v_cndmask_b32_e64 v69, v69, v87, s[12:13]
	v_cndmask_b32_e64 v68, v68, v86, s[12:13]
	v_cndmask_b32_e64 v67, v67, v89, s[12:13]
	v_cndmask_b32_e64 v66, v66, v88, s[12:13]
	v_pk_add_f32 v[86:87], v[62:63], s[84:85] op_sel_hi:[1,0]
	v_pk_add_f32 v[88:89], v[60:61], s[84:85] op_sel_hi:[1,0]
	v_cndmask_b32_e64 v63, v63, v87, s[10:11]
	v_cndmask_b32_e64 v62, v62, v86, s[10:11]
	v_cndmask_b32_e64 v61, v61, v89, s[10:11]
	v_cndmask_b32_e64 v60, v60, v88, s[10:11]
	v_pk_add_f32 v[86:87], v[58:59], s[84:85] op_sel_hi:[1,0]
	v_pk_add_f32 v[88:89], v[56:57], s[84:85] op_sel_hi:[1,0]
	v_cndmask_b32_e64 v59, v59, v87, s[8:9]
	v_cndmask_b32_e64 v58, v58, v86, s[8:9]
	v_cndmask_b32_e64 v57, v57, v89, s[8:9]
	v_cndmask_b32_e64 v56, v56, v88, s[8:9]
	v_pk_add_f32 v[86:87], v[54:55], s[84:85] op_sel_hi:[1,0]
	v_pk_add_f32 v[88:89], v[52:53], s[84:85] op_sel_hi:[1,0]
	v_cndmask_b32_e64 v55, v55, v87, s[6:7]
	v_cndmask_b32_e64 v54, v54, v86, s[6:7]
	v_cndmask_b32_e64 v53, v53, v89, s[6:7]
	v_cndmask_b32_e64 v52, v52, v88, s[6:7]
